# router pass-2 loops: packed f32 VALU between the MFMAs (feeding their A operands) split into scalar pairs
# speedup vs baseline: 1.0102x; 1.0102x over previous
.Lrtpf_skip_a:
	v_lshlrev_b32_e32 v90, 16, v44
	v_and_b32_e32 v91, 0xffff0000, v44
	v_mul_f32_e32 v90, v82, v90
	v_mul_f32_e32 v91, v83, v91
	s_waitcnt lgkmcnt(1)
	v_fma_f32 v90, v90, v114, v48
	v_fma_f32 v91, v91, v115, v49
	v_lshlrev_b32_e32 v114, 16, v45
	v_and_b32_e32 v115, 0xffff0000, v45
	v_mul_f32_e32 v114, v82, v114
	v_mul_f32_e32 v115, v83, v115
	v_cvt_pk_bf16_f32 v44, v90, v91
	v_fma_f32 v114, v114, v116, v50
	v_fma_f32 v115, v115, v117, v51
	v_lshlrev_b32_e32 v48, 16, v44
	v_cvt_pk_bf16_f32 v45, v114, v115
	v_and_b32_e32 v49, 0xffff0000, v44
	v_lshlrev_b32_e32 v50, 16, v45
	v_and_b32_e32 v51, 0xffff0000, v45
	v_sub_f32_e32 v48, v90, v48
	v_sub_f32_e32 v49, v91, v49
	v_sub_f32_e32 v50, v114, v50
	v_sub_f32_e32 v51, v115, v51
	v_cvt_pk_bf16_f32 v48, v48, v49
	v_cvt_pk_bf16_f32 v49, v50, v51
	v_lshlrev_b32_e32 v50, 16, v46
	v_and_b32_e32 v51, 0xffff0000, v46
	v_lshlrev_b32_e32 v116, 16, v47
	v_and_b32_e32 v117, 0xffff0000, v47
	v_mul_f32_e32 v50, v82, v50
	v_mul_f32_e32 v51, v83, v51
	v_mul_f32_e32 v116, v82, v116
	v_mul_f32_e32 v117, v83, v117
	s_waitcnt lgkmcnt(0)
	v_fma_f32 v110, v50, v118, v110
	v_fma_f32 v111, v51, v119, v111
	v_fma_f32 v112, v116, v120, v112
	v_fma_f32 v113, v117, v121, v113
	v_cvt_pk_bf16_f32 v46, v110, v111
	v_cvt_pk_bf16_f32 v47, v112, v113
	v_lshlrev_b32_e32 v50, 16, v46
	v_and_b32_e32 v51, 0xffff0000, v46
	v_lshlrev_b32_e32 v116, 16, v47
	v_and_b32_e32 v117, 0xffff0000, v47
	v_sub_f32_e32 v50, v110, v50
	v_sub_f32_e32 v51, v111, v51
	v_sub_f32_e32 v116, v112, v116
	v_sub_f32_e32 v117, v113, v117
	v_cvt_pk_bf16_f32 v50, v50, v51
	v_cvt_pk_bf16_f32 v51, v116, v117
	v_mov_b32_e32 v117, 0
	v_cvt_pk_fp8_f32 v117, v110, v111
	v_mov_b32_e32 v116, 0
	v_cvt_pk_fp8_f32 v116, v90, v91
	v_lshl_add_u64 v[90:91], s[52:53], 0, v[86:87]
	v_cvt_pk_fp8_f32 v117, v112, v113 op_sel:[0,0,1]
	ds_read_b128 v[110:113], v72
	v_cvt_pk_fp8_f32 v116, v114, v115 op_sel:[0,0,1]
	s_waitcnt lgkmcnt(0)
	v_mfma_f32_16x16x32_bf16 v[4:7], v[44:47], v[110:113], v[4:7]
	global_store_dwordx2 v[90:91], v[116:117], off offset:-64
	ds_read_b128 v[114:117], v74
	v_lshl_add_u64 v[86:87], v[86:87], 0, s[50:51]
	v_mfma_f32_16x16x32_bf16 v[4:7], v[48:51], v[110:113], v[4:7]
	ds_read_b128 v[110:113], v72 offset:32768
	v_add_u32_e32 v72, 0x18000, v72
	s_waitcnt lgkmcnt(0)
	v_mfma_f32_16x16x32_bf16 v[0:3], v[44:47], v[110:113], v[0:3]
	v_mfma_f32_16x16x32_bf16 v[4:7], v[44:47], v[114:117], v[4:7]
	ds_read_b128 v[114:117], v72
	v_mfma_f32_16x16x32_bf16 v[0:3], v[48:51], v[110:113], v[0:3]
	v_lshlrev_b32_e32 v110, 16, v32
	v_and_b32_e32 v111, 0xffff0000, v32
	v_add_u32_e32 v48, 0x20090, v70
	s_waitcnt lgkmcnt(0)
	v_mfma_f32_16x16x32_bf16 v[0:3], v[44:47], v[114:117], v[0:3]
	v_add_u32_e32 v44, 0x20080, v70
	ds_read_b128 v[44:47], v44
	ds_read_b128 v[48:51], v48
	v_mul_f32_e32 v110, v82, v110
	v_mul_f32_e32 v111, v83, v111
	s_waitcnt lgkmcnt(1)
	v_fma_f32 v44, v110, v44, v40
	v_fma_f32 v45, v111, v45, v41
	v_lshlrev_b32_e32 v110, 16, v33
	v_and_b32_e32 v111, 0xffff0000, v33
	v_mul_f32_e32 v110, v82, v110
	v_mul_f32_e32 v111, v83, v111
	v_cvt_pk_bf16_f32 v32, v44, v45
	v_fma_f32 v46, v110, v46, v42
	v_fma_f32 v47, v111, v47, v43
	v_lshlrev_b32_e32 v40, 16, v32
	v_cvt_pk_bf16_f32 v33, v46, v47
	v_and_b32_e32 v41, 0xffff0000, v32
	v_lshlrev_b32_e32 v42, 16, v33
	v_and_b32_e32 v43, 0xffff0000, v33
	v_sub_f32_e32 v40, v44, v40
	v_sub_f32_e32 v41, v45, v41
	v_sub_f32_e32 v42, v46, v42
	v_sub_f32_e32 v43, v47, v43
	v_cvt_pk_bf16_f32 v40, v40, v41
	v_cvt_pk_bf16_f32 v41, v42, v43
	v_lshlrev_b32_e32 v42, 16, v34
	v_and_b32_e32 v43, 0xffff0000, v34
	v_mul_f32_e32 v42, v82, v42
	v_mul_f32_e32 v43, v83, v43
	s_waitcnt lgkmcnt(0)
	v_fma_f32 v36, v42, v48, v36
	v_fma_f32 v37, v43, v49, v37
	v_lshlrev_b32_e32 v48, 16, v35
	v_and_b32_e32 v49, 0xffff0000, v35
	v_mul_f32_e32 v48, v82, v48
	v_mul_f32_e32 v49, v83, v49
	v_cvt_pk_bf16_f32 v34, v36, v37
	v_fma_f32 v38, v48, v50, v38
	v_fma_f32 v39, v49, v51, v39
	v_lshlrev_b32_e32 v42, 16, v34
	v_cvt_pk_bf16_f32 v35, v38, v39
	v_and_b32_e32 v43, 0xffff0000, v34
	v_lshlrev_b32_e32 v48, 16, v35
	v_and_b32_e32 v49, 0xffff0000, v35
	v_sub_f32_e32 v42, v36, v42
	v_sub_f32_e32 v43, v37, v43
	v_sub_f32_e32 v48, v38, v48
	v_sub_f32_e32 v49, v39, v49
	v_cvt_pk_bf16_f32 v42, v42, v43
	v_cvt_pk_bf16_f32 v43, v48, v49
	v_mov_b32_e32 v48, 0
	v_mov_b32_e32 v49, 0
	v_cvt_pk_fp8_f32 v48, v44, v45
	v_cvt_pk_fp8_f32 v49, v36, v37
	v_cvt_pk_fp8_f32 v48, v46, v47 op_sel:[0,0,1]
	v_cvt_pk_fp8_f32 v49, v38, v39 op_sel:[0,0,1]
	global_store_dwordx2 v[90:91], v[48:49], off offset:-32
	v_add_u32_e32 v48, 0, v64
	ds_read_b128 v[36:39], v48
	s_waitcnt lgkmcnt(0)
	v_mfma_f32_16x16x32_bf16 v[4:7], v[32:35], v[36:39], v[4:7]
	v_add_u32_e32 v44, 0x10000, v48
	ds_read_b128 v[44:47], v44
	v_add_u32_e32 v64, 0x100, v64
	v_mfma_f32_16x16x32_bf16 v[4:7], v[40:43], v[36:39], v[4:7]
	ds_read_b128 v[36:39], v48 offset:32768
	s_waitcnt lgkmcnt(0)
	v_mfma_f32_16x16x32_bf16 v[0:3], v[32:35], v[36:39], v[0:3]
	v_mfma_f32_16x16x32_bf16 v[4:7], v[32:35], v[44:47], v[4:7]
	v_add_u32_e32 v44, 0x18000, v48
	ds_read_b128 v[44:47], v44
	v_mfma_f32_16x16x32_bf16 v[0:3], v[40:43], v[36:39], v[0:3]
	v_lshlrev_b32_e32 v40, 16, v20
	v_and_b32_e32 v41, 0xffff0000, v20
	v_add_u32_e32 v36, 0x20110, v70
	s_waitcnt lgkmcnt(0)
	v_mfma_f32_16x16x32_bf16 v[0:3], v[32:35], v[44:47], v[0:3]
	v_add_u32_e32 v32, 0x20100, v70
	ds_read_b128 v[32:35], v32
	ds_read_b128 v[36:39], v36
	v_mul_f32_e32 v40, v82, v40
	v_mul_f32_e32 v41, v83, v41
	s_waitcnt lgkmcnt(1)
	v_fma_f32 v32, v40, v32, v28
	v_fma_f32 v33, v41, v33, v29
	v_lshlrev_b32_e32 v40, 16, v21
	v_and_b32_e32 v41, 0xffff0000, v21
	v_mul_f32_e32 v40, v82, v40
	v_mul_f32_e32 v41, v83, v41
	v_cvt_pk_bf16_f32 v20, v32, v33
	v_fma_f32 v34, v40, v34, v30
	v_fma_f32 v35, v41, v35, v31
	v_lshlrev_b32_e32 v28, 16, v20
	v_cvt_pk_bf16_f32 v21, v34, v35
	v_and_b32_e32 v29, 0xffff0000, v20
	v_lshlrev_b32_e32 v30, 16, v21
	v_and_b32_e32 v31, 0xffff0000, v21
	v_sub_f32_e32 v28, v32, v28
	v_sub_f32_e32 v29, v33, v29
	v_sub_f32_e32 v30, v34, v30
	v_sub_f32_e32 v31, v35, v31
	v_cvt_pk_bf16_f32 v28, v28, v29
	v_cvt_pk_bf16_f32 v29, v30, v31
	v_lshlrev_b32_e32 v30, 16, v22
	v_and_b32_e32 v31, 0xffff0000, v22
	v_mul_f32_e32 v30, v82, v30
	v_mul_f32_e32 v31, v83, v31
	s_waitcnt lgkmcnt(0)
	v_fma_f32 v24, v30, v36, v24
	v_fma_f32 v25, v31, v37, v25
	v_lshlrev_b32_e32 v36, 16, v23
	v_and_b32_e32 v37, 0xffff0000, v23
	v_mul_f32_e32 v36, v82, v36
	v_mul_f32_e32 v37, v83, v37
	v_cvt_pk_bf16_f32 v22, v24, v25
	v_fma_f32 v26, v36, v38, v26
	v_fma_f32 v27, v37, v39, v27
	v_lshlrev_b32_e32 v30, 16, v22
	v_cvt_pk_bf16_f32 v23, v26, v27
	v_and_b32_e32 v31, 0xffff0000, v22
	v_lshlrev_b32_e32 v36, 16, v23
	v_and_b32_e32 v37, 0xffff0000, v23
	v_sub_f32_e32 v30, v24, v30
	v_sub_f32_e32 v31, v25, v31
	v_sub_f32_e32 v36, v26, v36
	v_sub_f32_e32 v37, v27, v37
	v_cvt_pk_bf16_f32 v30, v30, v31
	v_cvt_pk_bf16_f32 v31, v36, v37
	v_mov_b32_e32 v36, 0
	v_mov_b32_e32 v37, 0
	v_cvt_pk_fp8_f32 v36, v32, v33
	v_cvt_pk_fp8_f32 v37, v24, v25
	v_cvt_pk_fp8_f32 v36, v34, v35 op_sel:[0,0,1]
	v_cvt_pk_fp8_f32 v37, v26, v27 op_sel:[0,0,1]
	global_store_dwordx2 v[90:91], v[36:37], off
	v_add_u32_e32 v36, 0, v66
	ds_read_b128 v[24:27], v36
	s_waitcnt lgkmcnt(0)
	v_mfma_f32_16x16x32_bf16 v[4:7], v[20:23], v[24:27], v[4:7]
	v_add_u32_e32 v32, 0x10000, v36
	ds_read_b128 v[32:35], v32
	v_add_u32_e32 v66, 0x100, v66
	v_mfma_f32_16x16x32_bf16 v[4:7], v[28:31], v[24:27], v[4:7]
	ds_read_b128 v[24:27], v36 offset:32768
	s_waitcnt lgkmcnt(0)
	v_mfma_f32_16x16x32_bf16 v[0:3], v[20:23], v[24:27], v[0:3]
	v_mfma_f32_16x16x32_bf16 v[4:7], v[20:23], v[32:35], v[4:7]
	v_add_u32_e32 v32, 0x18000, v36
	ds_read_b128 v[32:35], v32
	v_mfma_f32_16x16x32_bf16 v[0:3], v[28:31], v[24:27], v[0:3]
	v_lshlrev_b32_e32 v28, 16, v8
	v_and_b32_e32 v29, 0xffff0000, v8
	v_add_u32_e32 v24, 0x20190, v70
	s_waitcnt lgkmcnt(0)
	v_mfma_f32_16x16x32_bf16 v[0:3], v[20:23], v[32:35], v[0:3]
	v_add_u32_e32 v20, 0x20180, v70
	ds_read_b128 v[20:23], v20
	ds_read_b128 v[24:27], v24
	v_mul_f32_e32 v28, v82, v28
	v_mul_f32_e32 v29, v83, v29
	s_waitcnt lgkmcnt(1)
	v_fma_f32 v20, v28, v20, v16
	v_fma_f32 v21, v29, v21, v17
	v_lshlrev_b32_e32 v28, 16, v9
	v_and_b32_e32 v29, 0xffff0000, v9
	v_mul_f32_e32 v28, v82, v28
	v_mul_f32_e32 v29, v83, v29
	v_cvt_pk_bf16_f32 v8, v20, v21
	v_fma_f32 v22, v28, v22, v18
	v_fma_f32 v23, v29, v23, v19
	v_lshlrev_b32_e32 v16, 16, v8
	v_cvt_pk_bf16_f32 v9, v22, v23
	v_and_b32_e32 v17, 0xffff0000, v8
	v_lshlrev_b32_e32 v18, 16, v9
	v_and_b32_e32 v19, 0xffff0000, v9
	v_sub_f32_e32 v16, v20, v16
	v_sub_f32_e32 v17, v21, v17
	v_sub_f32_e32 v18, v22, v18
	v_sub_f32_e32 v19, v23, v19
	v_cvt_pk_bf16_f32 v16, v16, v17
	v_cvt_pk_bf16_f32 v17, v18, v19
	v_lshlrev_b32_e32 v18, 16, v10
	v_and_b32_e32 v19, 0xffff0000, v10
	v_mul_f32_e32 v18, v82, v18
	v_mul_f32_e32 v19, v83, v19
	s_waitcnt lgkmcnt(0)
	v_fma_f32 v12, v18, v24, v12
	v_fma_f32 v13, v19, v25, v13
	v_lshlrev_b32_e32 v24, 16, v11
	v_and_b32_e32 v25, 0xffff0000, v11
	v_mul_f32_e32 v24, v82, v24
	v_mul_f32_e32 v25, v83, v25
	v_cvt_pk_bf16_f32 v10, v12, v13
	v_fma_f32 v14, v24, v26, v14
	v_fma_f32 v15, v25, v27, v15
	v_lshlrev_b32_e32 v18, 16, v10
	v_cvt_pk_bf16_f32 v11, v14, v15
	v_and_b32_e32 v19, 0xffff0000, v10
	v_lshlrev_b32_e32 v24, 16, v11
	v_and_b32_e32 v25, 0xffff0000, v11
	v_sub_f32_e32 v18, v12, v18
	v_sub_f32_e32 v19, v13, v19
	v_sub_f32_e32 v24, v14, v24
	v_sub_f32_e32 v25, v15, v25
	v_cvt_pk_bf16_f32 v18, v18, v19
	v_cvt_pk_bf16_f32 v19, v24, v25
	v_mov_b32_e32 v24, 0
	v_mov_b32_e32 v25, 0
	v_cvt_pk_fp8_f32 v24, v20, v21
	v_cvt_pk_fp8_f32 v25, v12, v13
	v_cvt_pk_fp8_f32 v24, v22, v23 op_sel:[0,0,1]
	v_cvt_pk_fp8_f32 v25, v14, v15 op_sel:[0,0,1]
	global_store_dwordx2 v[90:91], v[24:25], off offset:32
	v_add_u32_e32 v24, 0, v68
	ds_read_b128 v[12:15], v24
	s_waitcnt lgkmcnt(0)
	v_mfma_f32_16x16x32_bf16 v[4:7], v[8:11], v[12:15], v[4:7]
	v_add_u32_e32 v20, 0x10000, v24
	ds_read_b128 v[20:23], v20
	v_add_u32_e32 v68, 0x100, v68
	v_mfma_f32_16x16x32_bf16 v[4:7], v[16:19], v[12:15], v[4:7]
	ds_read_b128 v[12:15], v24 offset:32768
	s_waitcnt lgkmcnt(0)
	v_mfma_f32_16x16x32_bf16 v[0:3], v[8:11], v[12:15], v[0:3]
	v_mfma_f32_16x16x32_bf16 v[4:7], v[8:11], v[20:23], v[4:7]
	v_add_u32_e32 v20, 0x18000, v24
	ds_read_b128 v[20:23], v20
	v_mfma_f32_16x16x32_bf16 v[0:3], v[16:19], v[12:15], v[0:3]
	s_waitcnt lgkmcnt(0)
	v_mfma_f32_16x16x32_bf16 v[0:3], v[8:11], v[20:23], v[0:3]
	s_cbranch_scc0 .LBB0_581
	global_load_dword v8, v[60:61], off
	global_load_dword v9, v[60:61], off offset:64
	s_waitcnt vmcnt(1)
	v_add_f32_e32 v4, v4, v8
	s_waitcnt vmcnt(0)
	s_nop 1
	v_add_f32_e32 v0, v0, v9
	v_add_f32_e32 v5, v5, v8
	v_add_f32_e32 v6, v6, v8
	v_add_f32_e32 v7, v7, v8
	v_add_f32_e32 v1, v1, v9
	v_add_f32_e32 v2, v2, v9
	v_add_f32_e32 v3, v3, v9
	ds_write2_b32 v95, v4, v0 offset1:16
	ds_write2_b32 v95, v5, v1 offset0:32 offset1:48
	ds_write2_b32 v95, v6, v2 offset0:64 offset1:80
	ds_write2_b32 v95, v7, v3 offset0:96 offset1:112
	ds_read_b128 v[28:31], v107
	ds_read_b128 v[24:27], v107 offset:16
	ds_read_b128 v[20:23], v107 offset:32
	ds_read_b128 v[16:19], v107 offset:48
	ds_read_b128 v[12:15], v107 offset:64
	ds_read_b128 v[8:11], v107 offset:80
	ds_read_b128 v[4:7], v107 offset:96
	ds_read_b128 v[0:3], v107 offset:112
	s_waitcnt lgkmcnt(7)
	v_mov_b32_e32 v52, v28
	s_waitcnt lgkmcnt(3)
	v_mov_b32_e32 v32, v12
	s_and_saveexec_b64 s[48:49], s[6:7]
	s_cbranch_execz .LBB0_588
	v_cmp_lt_i32_e32 vcc, 1, v94
	s_mov_b64 s[54:55], 0
	s_and_saveexec_b64 s[50:51], vcc
	s_xor_b64 s[56:57], exec, s[50:51]
	s_cbranch_execnz .LBB0_655
	s_andn2_saveexec_b64 s[56:57], s[56:57]
	s_cbranch_execnz .LBB0_658

.Lrtpf_skip_b:
	v_lshlrev_b32_e32 v90, 16, v44
	v_and_b32_e32 v91, 0xffff0000, v44
	v_mul_f32_e32 v90, v82, v90
	v_mul_f32_e32 v91, v83, v91
	s_waitcnt lgkmcnt(1)
	v_fma_f32 v90, v90, v114, v48
	v_fma_f32 v91, v91, v115, v49
	v_lshlrev_b32_e32 v114, 16, v45
	v_and_b32_e32 v115, 0xffff0000, v45
	v_mul_f32_e32 v114, v82, v114
	v_mul_f32_e32 v115, v83, v115
	v_cvt_pk_bf16_f32 v44, v90, v91
	v_fma_f32 v114, v114, v116, v50
	v_fma_f32 v115, v115, v117, v51
	v_lshlrev_b32_e32 v48, 16, v44
	v_cvt_pk_bf16_f32 v45, v114, v115
	v_and_b32_e32 v49, 0xffff0000, v44
	v_lshlrev_b32_e32 v50, 16, v45
	v_and_b32_e32 v51, 0xffff0000, v45
	v_sub_f32_e32 v48, v90, v48
	v_sub_f32_e32 v49, v91, v49
	v_sub_f32_e32 v50, v114, v50
	v_sub_f32_e32 v51, v115, v51
	v_cvt_pk_bf16_f32 v48, v48, v49
	v_cvt_pk_bf16_f32 v49, v50, v51
	v_lshlrev_b32_e32 v50, 16, v46
	v_and_b32_e32 v51, 0xffff0000, v46
	v_lshlrev_b32_e32 v116, 16, v47
	v_and_b32_e32 v117, 0xffff0000, v47
	v_mul_f32_e32 v50, v82, v50
	v_mul_f32_e32 v51, v83, v51
	v_mul_f32_e32 v116, v82, v116
	v_mul_f32_e32 v117, v83, v117
	s_waitcnt lgkmcnt(0)
	v_fma_f32 v110, v50, v118, v110
	v_fma_f32 v111, v51, v119, v111
	v_fma_f32 v112, v116, v120, v112
	v_fma_f32 v113, v117, v121, v113
	v_cvt_pk_bf16_f32 v46, v110, v111
	v_cvt_pk_bf16_f32 v47, v112, v113
	v_lshlrev_b32_e32 v50, 16, v46
	v_and_b32_e32 v51, 0xffff0000, v46
	v_lshlrev_b32_e32 v116, 16, v47
	v_and_b32_e32 v117, 0xffff0000, v47
	v_sub_f32_e32 v50, v110, v50
	v_sub_f32_e32 v51, v111, v51
	v_sub_f32_e32 v116, v112, v116
	v_sub_f32_e32 v117, v113, v117
	v_cvt_pk_bf16_f32 v50, v50, v51
	v_cvt_pk_bf16_f32 v51, v116, v117
	v_mov_b32_e32 v117, 0
	v_cvt_pk_fp8_f32 v117, v110, v111
	v_mov_b32_e32 v116, 0
	v_cvt_pk_fp8_f32 v116, v90, v91
	v_lshl_add_u64 v[90:91], s[52:53], 0, v[86:87]
	v_cvt_pk_fp8_f32 v117, v112, v113 op_sel:[0,0,1]
	ds_read_b128 v[110:113], v72
	v_cvt_pk_fp8_f32 v116, v114, v115 op_sel:[0,0,1]
	s_waitcnt lgkmcnt(0)
	v_mfma_f32_16x16x32_bf16 v[4:7], v[44:47], v[110:113], v[4:7]
	global_store_dwordx2 v[90:91], v[116:117], off offset:-64
	ds_read_b128 v[114:117], v74
	v_lshl_add_u64 v[86:87], v[86:87], 0, s[50:51]
	v_mfma_f32_16x16x32_bf16 v[4:7], v[48:51], v[110:113], v[4:7]
	ds_read_b128 v[110:113], v72 offset:32768
	v_add_u32_e32 v72, 0x18000, v72
	s_waitcnt lgkmcnt(0)
	v_mfma_f32_16x16x32_bf16 v[0:3], v[44:47], v[110:113], v[0:3]
	v_mfma_f32_16x16x32_bf16 v[4:7], v[44:47], v[114:117], v[4:7]
	ds_read_b128 v[114:117], v72
	v_mfma_f32_16x16x32_bf16 v[0:3], v[48:51], v[110:113], v[0:3]
	v_lshlrev_b32_e32 v110, 16, v32
	v_and_b32_e32 v111, 0xffff0000, v32
	v_add_u32_e32 v48, 0x20090, v70
	s_waitcnt lgkmcnt(0)
	v_mfma_f32_16x16x32_bf16 v[0:3], v[44:47], v[114:117], v[0:3]
	v_add_u32_e32 v44, 0x20080, v70
	ds_read_b128 v[44:47], v44
	ds_read_b128 v[48:51], v48
	v_mul_f32_e32 v110, v82, v110
	v_mul_f32_e32 v111, v83, v111
	s_waitcnt lgkmcnt(1)
	v_fma_f32 v44, v110, v44, v40
	v_fma_f32 v45, v111, v45, v41
	v_lshlrev_b32_e32 v110, 16, v33
	v_and_b32_e32 v111, 0xffff0000, v33
	v_mul_f32_e32 v110, v82, v110
	v_mul_f32_e32 v111, v83, v111
	v_cvt_pk_bf16_f32 v32, v44, v45
	v_fma_f32 v46, v110, v46, v42
	v_fma_f32 v47, v111, v47, v43
	v_lshlrev_b32_e32 v40, 16, v32
	v_cvt_pk_bf16_f32 v33, v46, v47
	v_and_b32_e32 v41, 0xffff0000, v32
	v_lshlrev_b32_e32 v42, 16, v33
	v_and_b32_e32 v43, 0xffff0000, v33
	v_sub_f32_e32 v40, v44, v40
	v_sub_f32_e32 v41, v45, v41
	v_sub_f32_e32 v42, v46, v42
	v_sub_f32_e32 v43, v47, v43
	v_cvt_pk_bf16_f32 v40, v40, v41
	v_cvt_pk_bf16_f32 v41, v42, v43
	v_lshlrev_b32_e32 v42, 16, v34
	v_and_b32_e32 v43, 0xffff0000, v34
	v_mul_f32_e32 v42, v82, v42
	v_mul_f32_e32 v43, v83, v43
	s_waitcnt lgkmcnt(0)
	v_fma_f32 v36, v42, v48, v36
	v_fma_f32 v37, v43, v49, v37
	v_lshlrev_b32_e32 v48, 16, v35
	v_and_b32_e32 v49, 0xffff0000, v35
	v_mul_f32_e32 v48, v82, v48
	v_mul_f32_e32 v49, v83, v49
	v_cvt_pk_bf16_f32 v34, v36, v37
	v_fma_f32 v38, v48, v50, v38
	v_fma_f32 v39, v49, v51, v39
	v_lshlrev_b32_e32 v42, 16, v34
	v_cvt_pk_bf16_f32 v35, v38, v39
	v_and_b32_e32 v43, 0xffff0000, v34
	v_lshlrev_b32_e32 v48, 16, v35
	v_and_b32_e32 v49, 0xffff0000, v35
	v_sub_f32_e32 v42, v36, v42
	v_sub_f32_e32 v43, v37, v43
	v_sub_f32_e32 v48, v38, v48
	v_sub_f32_e32 v49, v39, v49
	v_cvt_pk_bf16_f32 v42, v42, v43
	v_cvt_pk_bf16_f32 v43, v48, v49
	v_mov_b32_e32 v48, 0
	v_mov_b32_e32 v49, 0
	v_cvt_pk_fp8_f32 v48, v44, v45
	v_cvt_pk_fp8_f32 v49, v36, v37
	v_cvt_pk_fp8_f32 v48, v46, v47 op_sel:[0,0,1]
	v_cvt_pk_fp8_f32 v49, v38, v39 op_sel:[0,0,1]
	global_store_dwordx2 v[90:91], v[48:49], off offset:-32
	v_add_u32_e32 v48, 0, v64
	ds_read_b128 v[36:39], v48
	s_waitcnt lgkmcnt(0)
	v_mfma_f32_16x16x32_bf16 v[4:7], v[32:35], v[36:39], v[4:7]
	v_add_u32_e32 v44, 0x10000, v48
	ds_read_b128 v[44:47], v44
	v_add_u32_e32 v64, 0x100, v64
	v_mfma_f32_16x16x32_bf16 v[4:7], v[40:43], v[36:39], v[4:7]
	ds_read_b128 v[36:39], v48 offset:32768
	s_waitcnt lgkmcnt(0)
	v_mfma_f32_16x16x32_bf16 v[0:3], v[32:35], v[36:39], v[0:3]
	v_mfma_f32_16x16x32_bf16 v[4:7], v[32:35], v[44:47], v[4:7]
	v_add_u32_e32 v44, 0x18000, v48
	ds_read_b128 v[44:47], v44
	v_mfma_f32_16x16x32_bf16 v[0:3], v[40:43], v[36:39], v[0:3]
	v_lshlrev_b32_e32 v40, 16, v20
	v_and_b32_e32 v41, 0xffff0000, v20
	v_add_u32_e32 v36, 0x20110, v70
	s_waitcnt lgkmcnt(0)
	v_mfma_f32_16x16x32_bf16 v[0:3], v[32:35], v[44:47], v[0:3]
	v_add_u32_e32 v32, 0x20100, v70
	ds_read_b128 v[32:35], v32
	ds_read_b128 v[36:39], v36
	v_mul_f32_e32 v40, v82, v40
	v_mul_f32_e32 v41, v83, v41
	s_waitcnt lgkmcnt(1)
	v_fma_f32 v32, v40, v32, v28
	v_fma_f32 v33, v41, v33, v29
	v_lshlrev_b32_e32 v40, 16, v21
	v_and_b32_e32 v41, 0xffff0000, v21
	v_mul_f32_e32 v40, v82, v40
	v_mul_f32_e32 v41, v83, v41
	v_cvt_pk_bf16_f32 v20, v32, v33
	v_fma_f32 v34, v40, v34, v30
	v_fma_f32 v35, v41, v35, v31
	v_lshlrev_b32_e32 v28, 16, v20
	v_cvt_pk_bf16_f32 v21, v34, v35
	v_and_b32_e32 v29, 0xffff0000, v20
	v_lshlrev_b32_e32 v30, 16, v21
	v_and_b32_e32 v31, 0xffff0000, v21
	v_sub_f32_e32 v28, v32, v28
	v_sub_f32_e32 v29, v33, v29
	v_sub_f32_e32 v30, v34, v30
	v_sub_f32_e32 v31, v35, v31
	v_cvt_pk_bf16_f32 v28, v28, v29
	v_cvt_pk_bf16_f32 v29, v30, v31
	v_lshlrev_b32_e32 v30, 16, v22
	v_and_b32_e32 v31, 0xffff0000, v22
	v_mul_f32_e32 v30, v82, v30
	v_mul_f32_e32 v31, v83, v31
	s_waitcnt lgkmcnt(0)
	v_fma_f32 v24, v30, v36, v24
	v_fma_f32 v25, v31, v37, v25
	v_lshlrev_b32_e32 v36, 16, v23
	v_and_b32_e32 v37, 0xffff0000, v23
	v_mul_f32_e32 v36, v82, v36
	v_mul_f32_e32 v37, v83, v37
	v_cvt_pk_bf16_f32 v22, v24, v25
	v_fma_f32 v26, v36, v38, v26
	v_fma_f32 v27, v37, v39, v27
	v_lshlrev_b32_e32 v30, 16, v22
	v_cvt_pk_bf16_f32 v23, v26, v27
	v_and_b32_e32 v31, 0xffff0000, v22
	v_lshlrev_b32_e32 v36, 16, v23
	v_and_b32_e32 v37, 0xffff0000, v23
	v_sub_f32_e32 v30, v24, v30
	v_sub_f32_e32 v31, v25, v31
	v_sub_f32_e32 v36, v26, v36
	v_sub_f32_e32 v37, v27, v37
	v_cvt_pk_bf16_f32 v30, v30, v31
	v_cvt_pk_bf16_f32 v31, v36, v37
	v_mov_b32_e32 v36, 0
	v_mov_b32_e32 v37, 0
	v_cvt_pk_fp8_f32 v36, v32, v33
	v_cvt_pk_fp8_f32 v37, v24, v25
	v_cvt_pk_fp8_f32 v36, v34, v35 op_sel:[0,0,1]
	v_cvt_pk_fp8_f32 v37, v26, v27 op_sel:[0,0,1]
	global_store_dwordx2 v[90:91], v[36:37], off
	v_add_u32_e32 v36, 0, v66
	ds_read_b128 v[24:27], v36
	s_waitcnt lgkmcnt(0)
	v_mfma_f32_16x16x32_bf16 v[4:7], v[20:23], v[24:27], v[4:7]
	v_add_u32_e32 v32, 0x10000, v36
	ds_read_b128 v[32:35], v32
	v_add_u32_e32 v66, 0x100, v66
	v_mfma_f32_16x16x32_bf16 v[4:7], v[28:31], v[24:27], v[4:7]
	ds_read_b128 v[24:27], v36 offset:32768
	s_waitcnt lgkmcnt(0)
	v_mfma_f32_16x16x32_bf16 v[0:3], v[20:23], v[24:27], v[0:3]
	v_mfma_f32_16x16x32_bf16 v[4:7], v[20:23], v[32:35], v[4:7]
	v_add_u32_e32 v32, 0x18000, v36
	ds_read_b128 v[32:35], v32
	v_mfma_f32_16x16x32_bf16 v[0:3], v[28:31], v[24:27], v[0:3]
	v_lshlrev_b32_e32 v28, 16, v8
	v_and_b32_e32 v29, 0xffff0000, v8
	v_add_u32_e32 v24, 0x20190, v70
	s_waitcnt lgkmcnt(0)
	v_mfma_f32_16x16x32_bf16 v[0:3], v[20:23], v[32:35], v[0:3]
	v_add_u32_e32 v20, 0x20180, v70
	ds_read_b128 v[20:23], v20
	ds_read_b128 v[24:27], v24
	v_mul_f32_e32 v28, v82, v28
	v_mul_f32_e32 v29, v83, v29
	s_waitcnt lgkmcnt(1)
	v_fma_f32 v20, v28, v20, v16
	v_fma_f32 v21, v29, v21, v17
	v_lshlrev_b32_e32 v28, 16, v9
	v_and_b32_e32 v29, 0xffff0000, v9
	v_mul_f32_e32 v28, v82, v28
	v_mul_f32_e32 v29, v83, v29
	v_cvt_pk_bf16_f32 v8, v20, v21
	v_fma_f32 v22, v28, v22, v18
	v_fma_f32 v23, v29, v23, v19
	v_lshlrev_b32_e32 v16, 16, v8
	v_cvt_pk_bf16_f32 v9, v22, v23
	v_and_b32_e32 v17, 0xffff0000, v8
	v_lshlrev_b32_e32 v18, 16, v9
	v_and_b32_e32 v19, 0xffff0000, v9
	v_sub_f32_e32 v16, v20, v16
	v_sub_f32_e32 v17, v21, v17
	v_sub_f32_e32 v18, v22, v18
	v_sub_f32_e32 v19, v23, v19
	v_cvt_pk_bf16_f32 v16, v16, v17
	v_cvt_pk_bf16_f32 v17, v18, v19
	v_lshlrev_b32_e32 v18, 16, v10
	v_and_b32_e32 v19, 0xffff0000, v10
	v_mul_f32_e32 v18, v82, v18
	v_mul_f32_e32 v19, v83, v19
	s_waitcnt lgkmcnt(0)
	v_fma_f32 v12, v18, v24, v12
	v_fma_f32 v13, v19, v25, v13
	v_lshlrev_b32_e32 v24, 16, v11
	v_and_b32_e32 v25, 0xffff0000, v11
	v_mul_f32_e32 v24, v82, v24
	v_mul_f32_e32 v25, v83, v25
	v_cvt_pk_bf16_f32 v10, v12, v13
	v_fma_f32 v14, v24, v26, v14
	v_fma_f32 v15, v25, v27, v15
	v_lshlrev_b32_e32 v18, 16, v10
	v_cvt_pk_bf16_f32 v11, v14, v15
	v_and_b32_e32 v19, 0xffff0000, v10
	v_lshlrev_b32_e32 v24, 16, v11
	v_and_b32_e32 v25, 0xffff0000, v11
	v_sub_f32_e32 v18, v12, v18
	v_sub_f32_e32 v19, v13, v19
	v_sub_f32_e32 v24, v14, v24
	v_sub_f32_e32 v25, v15, v25
	v_cvt_pk_bf16_f32 v18, v18, v19
	v_cvt_pk_bf16_f32 v19, v24, v25
	v_mov_b32_e32 v24, 0
	v_mov_b32_e32 v25, 0
	v_cvt_pk_fp8_f32 v24, v20, v21
	v_cvt_pk_fp8_f32 v25, v12, v13
	v_cvt_pk_fp8_f32 v24, v22, v23 op_sel:[0,0,1]
	v_cvt_pk_fp8_f32 v25, v14, v15 op_sel:[0,0,1]
	global_store_dwordx2 v[90:91], v[24:25], off offset:32
	v_add_u32_e32 v24, 0, v68
	ds_read_b128 v[12:15], v24
	s_waitcnt lgkmcnt(0)
	v_mfma_f32_16x16x32_bf16 v[4:7], v[8:11], v[12:15], v[4:7]
	v_add_u32_e32 v20, 0x10000, v24
	ds_read_b128 v[20:23], v20
	v_add_u32_e32 v68, 0x100, v68
	v_mfma_f32_16x16x32_bf16 v[4:7], v[16:19], v[12:15], v[4:7]
	ds_read_b128 v[12:15], v24 offset:32768
	s_waitcnt lgkmcnt(0)
	v_mfma_f32_16x16x32_bf16 v[0:3], v[8:11], v[12:15], v[0:3]
	v_mfma_f32_16x16x32_bf16 v[4:7], v[8:11], v[20:23], v[4:7]
	v_add_u32_e32 v20, 0x18000, v24
	ds_read_b128 v[20:23], v20
	v_mfma_f32_16x16x32_bf16 v[0:3], v[16:19], v[12:15], v[0:3]
	s_waitcnt lgkmcnt(0)
	v_mfma_f32_16x16x32_bf16 v[0:3], v[8:11], v[20:23], v[0:3]
	s_cbranch_scc0 .LBB0_1663
	global_load_dword v8, v[60:61], off offset:128
	global_load_dword v9, v[60:61], off offset:192
	s_waitcnt vmcnt(1)
	v_add_f32_e32 v4, v4, v8
	s_waitcnt vmcnt(0)
	s_nop 1
	v_add_f32_e32 v0, v0, v9
	v_add_f32_e32 v5, v5, v8
	v_add_f32_e32 v6, v6, v8
	v_add_f32_e32 v7, v7, v8
	v_add_f32_e32 v1, v1, v9
	v_add_f32_e32 v2, v2, v9
	v_add_f32_e32 v3, v3, v9
	ds_write2_b32 v95, v4, v0 offset1:16
	ds_write2_b32 v95, v5, v1 offset0:32 offset1:48
	ds_write2_b32 v95, v6, v2 offset0:64 offset1:80
	ds_write2_b32 v95, v7, v3 offset0:96 offset1:112
	ds_read_b128 v[28:31], v107
	ds_read_b128 v[24:27], v107 offset:16
	ds_read_b128 v[20:23], v107 offset:32
	ds_read_b128 v[16:19], v107 offset:48
	ds_read_b128 v[12:15], v107 offset:64
	ds_read_b128 v[8:11], v107 offset:80
	ds_read_b128 v[4:7], v107 offset:96
	ds_read_b128 v[0:3], v107 offset:112
	s_waitcnt lgkmcnt(7)
	v_mov_b32_e32 v52, v28
	s_waitcnt lgkmcnt(3)
	v_mov_b32_e32 v32, v12
	s_and_saveexec_b64 s[48:49], s[6:7]
	s_cbranch_execz .LBB0_1670
	v_cmp_lt_i32_e32 vcc, 1, v94
	s_mov_b64 s[54:55], 0
	s_and_saveexec_b64 s[50:51], vcc
	s_xor_b64 s[56:57], exec, s[50:51]
	s_cbranch_execnz .LBB0_1737
	s_andn2_saveexec_b64 s[56:57], s[56:57]
	s_cbranch_execnz .LBB0_1740
